# P1: 72 converter workgroups; after converting they run the in-projection GEMM code on the last 128 tiles, the 184 GEMM workgroups do 16 tiles each
# baseline (speedup 1.0000x reference)
; #define LAS __attribute__((address_space(3)))
; __global__ void __launch_bounds__(NTHREADS, 2) mk_fwd(Args args) {
;     extern __shared__ __attribute__((aligned(16))) unsigned char lds[];
;     Frame F;
;     F.lds = (LAS unsigned char*)lds;
;     F.tid = threadIdx.x; F.lane = F.tid & 63; F.wave = __builtin_amdgcn_readfirstlane(F.tid >> 6);
;     F.G = gridDim.x; { const int bx = blockIdx.x; F.vcu = (F.G % 8 == 0) ? (bx % 8) * (F.G / 8) + bx / 8 : bx; }
;     F.ws = args.ws;
_Z6mk_fwd4Args:
	s_mov_b32 s92, s2
	s_mov_b32 s98, s2
	s_load_dword s2, s[0:1], 0xc8
	s_mov_b64 s[96:97], s[0:1]
	s_add_u32 s0, s96, 0xc8
	s_addc_u32 s1, s97, 0
	v_writelane_b32 v254, s0, 0
	s_nop 1
	v_writelane_b32 v254, s1, 1
	s_waitcnt lgkmcnt(0)
	s_and_b32 s0, s2, 7
	s_cmp_lg_u32 s0, 0
	s_mov_b32 s0, s92
	v_writelane_b32 v254, s0, 2
	s_cbranch_scc1 .LBB0_2
	s_ashr_i32 s1, s92, 31
	s_lshr_b32 s1, s1, 29
	s_add_i32 s1, s92, s1
	s_and_b32 s3, s1, -8
	s_ashr_i32 s0, s2, 3
	s_sub_i32 s3, s92, s3
	s_mul_i32 s0, s0, s3
	s_ashr_i32 s1, s1, 3
	s_add_i32 s0, s0, s1
	v_writelane_b32 v254, s0, 2

; #define LAS __attribute__((address_space(3)))
; __device__ __forceinline__ void conv_rest(Frame& F, const Args& a, int gw, int NGW) {
;     LAS unsigned* scr = (LAS unsigned*)(F.lds + F.wave * 13824);
;     bf16_t* Wpa = (bf16_t*)(F.ws + WS_WPA); bf16_t* Wpr = (bf16_t*)(F.ws + WS_WPR); bf16_t* Wout = (bf16_t*)(F.ws + WS_WOUT);
;     unsigned char* Wgu = (unsigned char*)(F.ws + WS_WGU); unsigned char* Wdn = (unsigned char*)(F.ws + WS_WDN);
;     constexpr int I_PA = (GW / 64) * (D / 32), I_PR = (D / 64) * (D / 32), I_OUT = I_PR, I_GU1 = (D / 128) * (4096 / 32), I_DN1 = (DFF / 128) * (D / 32);
;     constexpr int NITEMS = I_PA + I_PR + I_OUT;
;     for (int it = gw; it < NITEMS; it += NGW) {
;         int r = it;
;         if (r < I_PA) { transpose_item(a.in[7], GW, D, Wpa, CM_STD, r, scr, F.lane); continue; } r -= I_PA;
; __global__ void __launch_bounds__(NTHREADS, 2) mk_fwd(Args args) {
;     ...
;         const int nconv = (MK_NCONV * F.G) / 256, ngemm = F.G - nconv;
;         if ((int)blockIdx.x < ngemm) {
;             pg8::DenseSched S; S.init((const bf16_t*)(F.ws + WS_H), D, (const bf16_t*)(F.ws + WS_WIN), D, T, INW, ngemm, (int)blockIdx.x);
;             EpiInProj E{F.ws};
;             if (MK_RSYNC) pg8::gemm_phase<0, EpiInProj, pg8::DenseSched, 127, 127, true>(F.lds, S, E, &bar); else pg8::gemm_phase<0>(F.lds, S, E);
;         } else if (!MK_CONV_IN_P0) conv_rest(F, args, ((int)blockIdx.x - ngemm) * NWAVES + F.wave, nconv * NWAVES);
.LBB0_102:
	s_cmp_lt_i32 s88, 2
	s_cselect_b64 s[4:5], -1, 0
	s_and_b64 s[14:15], s[4:5], s[0:1]
	s_andn2_b64 vcc, exec, s[14:15]
	s_cbranch_vccnz .LBB0_282
	s_ashr_i32 s0, s2, 31
	s_lshr_b32 s0, s0, 30
	s_add_i32 s0, s2, s0
	s_movk_i32 s18, 72
	s_waitcnt vmcnt(6)
	v_mov_b32_e32 v18, v0
	s_sub_i32 s3, s2, s18
	s_cmp_ge_i32 s92, s3
	v_readfirstlane_b32 s4, v18
	s_mov_b64 s[0:1], -1
	s_mov_b32 s98, s92
	s_movk_i32 s99, 0xb80
	s_cbranch_scc0 .LBB0_126
	s_sub_i32 s0, s92, s3
	s_ashr_i32 s19, s4, 6
	s_lshl_b32 s0, s0, 3
	s_add_i32 s21, s19, s0
	s_mul_i32 s0, s19, 0x3600
	s_add_i32 s34, s0, 0
	s_load_dwordx2 s[8:9], s[96:97], 0x68
	s_load_dwordx2 s[0:1], s[96:97], 0x78
	s_waitcnt vmcnt(4)
	v_and_b32_e32 v2, 7, v18
	v_bfe_u32 v1, v18, 3, 3
	v_lshlrev_b32_e32 v164, 4, v2
	s_lshl_b32 s20, s18, 3
	v_lshl_add_u32 v3, v1, 2, s34
	v_mul_u32_u24_e32 v4, 0x210, v2
	v_mul_u32_u24_e32 v5, 0x84, v1
	s_waitcnt vmcnt(2)
	v_add_u32_e32 v6, s34, v164
	v_and_b32_e32 v19, 63, v18
	s_mov_b32 s11, 0
	v_or_b32_e32 v173, 8, v1
	v_or_b32_e32 v168, 16, v1
	v_or_b32_e32 v169, 24, v1
	v_and_b32_e32 v174, 4, v18
	s_cmpk_gt_i32 s21, 0x13ff
	v_add_u32_e32 v170, v3, v4
	v_add_u32_e32 v171, v6, v5
	s_cbranch_scc1 .LBB0_115
	v_mov_b32_e32 v3, 0
	s_load_dwordx4 s[4:7], s[96:97], 0x38
	s_load_dwordx2 s[12:13], s[96:97], 0x48
	v_mov_b32_e32 v165, v3
	v_lshl_add_u64 v[8:9], s[94:95], 0, v[164:165]
	s_mov_b64 s[16:17], 0x3e00000
	v_lshl_add_u64 v[4:5], v[8:9], 0, s[16:17]
	s_mov_b64 s[16:17], 0x3600000
	v_lshlrev_b32_e32 v20, 2, v2
	v_lshlrev_b32_e32 v2, 3, v2
	v_lshl_add_u64 v[6:7], v[8:9], 0, s[16:17]
	s_mov_b64 s[16:17], 0x3200000
	v_lshlrev_b32_e32 v21, 14, v1
	v_and_or_b32 v22, v2, 24, v174
	v_lshlrev_b32_e32 v23, 1, v1
	v_lshl_add_u64 v[8:9], v[8:9], 0, s[16:17]
	v_lshl_or_b32 v24, s21, 6, v2
	s_lshl_b32 s22, s20, 6
	s_lshl_b32 s23, s21, 5
	s_lshl_b32 s24, s20, 5
	s_movk_i32 s25, 0x2000
	s_mov_b32 s26, 0x20000
	s_mov_b32 s27, 0x22000
	s_mov_b32 s28, 0x40000
	s_mov_b32 s29, 0x42000
	s_mov_b32 s30, 0x60000
	s_mov_b32 s31, 0x62000
	v_add_u32_e32 v25, 0x420, v171
	v_add_u32_e32 v26, 0x428, v171
	v_add_u32_e32 v27, 0x840, v171
	v_add_u32_e32 v28, 0x848, v171
	v_add_u32_e32 v29, 0xc60, v171
	s_waitcnt vmcnt(1)
	v_add_u32_e32 v30, 0xc68, v171
	s_mov_b32 s33, s21
	s_branch .LBB0_107

; __global__ void __launch_bounds__(NTHREADS, 2) mk_fwd(Args args) {
;     ...
;         if ((int)blockIdx.x < ngemm) {
;             pg8::DenseSched S; S.init((const bf16_t*)(F.ws + WS_H), D, (const bf16_t*)(F.ws + WS_WIN), D, T, INW, ngemm, (int)blockIdx.x);
;             EpiInProj E{F.ws};
;             if (MK_RSYNC) pg8::gemm_phase<0, EpiInProj, pg8::DenseSched, 127, 127, true>(F.lds, S, E, &bar); else pg8::gemm_phase<0>(F.lds, S, E);
;         } else if (!MK_CONV_IN_P0) conv_rest(F, args, ((int)blockIdx.x - ngemm) * NWAVES + F.wave, nconv * NWAVES);
.LBB0_125:
	s_waitcnt lgkmcnt(0)
	s_waitcnt vmcnt(0)
	s_barrier
	s_mov_b32 s98, s92
	s_add_i32 s92, s92, 0xac8
	s_movk_i32 s3, 72
	s_movk_i32 s99, 0xc00
	s_mov_b64 s[0:1], -1

;     __device__ __forceinline__ const char* a_base(const Unit& u) const { return (const char*)A + (size_t)u.pm * BM * lda * 2; }
;     __device__ __forceinline__ const char* b_base(const Unit& u) const { return (const char*)Bt + (size_t)u.pn * BM * K * 2; }
;     __device__ __forceinline__ const char* b_base(const Unit& u) const { return (const char*)Bt + ((size_t)u.e * NB + (size_t)u.pn * BM) * K * 2; }
; #define PG8_RC() int R[2], C[2]; { int t_ = threadIdx.x; asm volatile("" : "+v"(t_)); _Pragma("unroll") for (int i = 0; i < 2; ++i) stage_rc(t_ * 16 + i * 8192, R[i], C[i]); }
;     ...
;     const unsigned ldsbase = (unsigned)__builtin_amdgcn_readfirstlane((int)((unsigned)(size_t)lds + (unsigned)wid * 1024u));
;     const int aoff = lds_byte(wr * 64 + fr, fq * 8), boff = lds_byte(wc * 32 + fr, fq * 8);
;     ...
;     constexpr int EST = HM ? Epi::kStoresHM : Epi::kStores;
;     ...
;     Unit cur, nxt; int ui = 0;
;     if (!S.next(0, cur)) return;
;     unsigned voffA[2][2];
;     { PG8_RC(); S.a_offs(cur, R, C, voffA); }
;     f32x4 acc[2][2][4][2];
; #pragma unroll
;     for (int a = 0; a < 2; ++a)
; #pragma unroll
;         for (int b = 0; b < 2; ++b)
; #pragma unroll
;             for (int m = 0; m < 4; ++m)
; #pragma unroll
;                 for (int n = 0; n < 2; ++n) acc[a][b][m][n] = (f32x4){0.f, 0.f, 0.f, 0.f};
;     bf16x8 At[4][2], B0[2][2], B1[2][2];
;     const char* cA = S.a_base(cur); const char* cB = S.b_base(cur);
;     const unsigned bias_lds = (unsigned)__builtin_amdgcn_readfirstlane((int)((unsigned)(size_t)lds + (unsigned)(AUX_OFF + 8192) + (unsigned)wid * 256u));
;     if constexpr (Epi::kBiasDMA) { if (lane < 16) glds16(E.bias_base(cur), E.bias_off(cur, wc, lane), bias_lds); }
;     const unsigned rowid_lds = (unsigned)__builtin_amdgcn_readfirstlane((int)((unsigned)(size_t)lds + (unsigned)AUX_OFF + (unsigned)wid * 512u));
;     if constexpr (Epi::kRowDMA) { if (lane < 32) glds16(E.row_base(cur), E.row_off(cur, wr, lane), rowid_lds); }
;     PG8_STAGEB(PG8_SB(0, 0), cB); PG8_STAGEB(PG8_SB(0, 1), cB + hstepB); PG8_STAGEA(PG8_SA(0, 0), cA, 0); if constexpr (!HM) PG8_STAGEA(PG8_SA(0, 1), cA, 1);
;     if (wr == 1) PG8_BAR;
;     if constexpr (HM) PG8_WAIT_V(0); else PG8_WAIT_V(2);
;     PG8_BAR;
;     PG8_STAGEB(PG8_SB(1, 0), cB + kstep); PG8_STAGEA(PG8_SA(1, 0), cA + kstep, 0); PG8_STAGEB(PG8_SB(1, 1), cB + hstepB + kstep);
;     PG8_WAIT_V(6); PG8_BAR;
.LBB0_132:
	v_bfe_u32 v6, v2, 4, 2
	v_and_b32_e32 v3, 15, v2
	v_lshlrev_b32_e32 v4, 4, v6
	v_lshlrev_b32_e32 v2, 2, v2
	s_and_b32 s8, s6, 3
	v_lshl_or_b32 v161, s0, 6, v3
	v_lshl_or_b32 v3, v3, 6, v4
	s_lshl_b32 s0, s0, 13
	v_and_b32_e32 v2, 32, v2
	v_bitop3_b32 v8, v3, s0, v2 bitop3:0xde
	s_lshl_b32 s0, s8, 12
	s_add_u32 s62, s94, 0x50600000
	s_addc_u32 s63, s95, 0
	s_ashr_i32 s64, s3, 31
	s_ashr_i32 s65, s92, 31
	v_bitop3_b32 v3, v3, s0, v2 bitop3:0xde
	s_add_u32 s0, s54, 0x80
	s_waitcnt vmcnt(2)
	s_barrier
	s_addc_u32 s1, s55, 0
	s_add_i32 s66, s29, 0x18000
	s_mov_b32 s6, m0
	s_mov_b32 m0, s66
	s_nop 0
	global_load_lds_dwordx4 v1, s[0:1]
	s_mov_b32 m0, s6
	s_add_i32 s67, s29, 0x1a000
	s_mov_b32 s6, m0
	s_mov_b32 m0, s67
	s_nop 0
	global_load_lds_dwordx4 v156, s[0:1]
	s_mov_b32 m0, s6
	s_add_u32 s0, s12, 0x80
	s_addc_u32 s1, s13, 0
	s_add_i32 s68, s29, 0x8000
	s_mov_b32 s6, m0
	s_mov_b32 m0, s68
	s_nop 0
	global_load_lds_dwordx4 v157, s[0:1]
	s_mov_b32 m0, s6
	s_add_i32 s69, s29, 0xa000
	s_mov_b32 s6, m0
	s_mov_b32 m0, s69
	s_nop 0
	global_load_lds_dwordx4 v158, s[0:1]
	s_mov_b32 m0, s6
	s_add_u32 s0, s54, 0x80080
	v_lshlrev_b32_e32 v2, 2, v6
	s_addc_u32 s1, s55, 0
	s_add_i32 s70, s29, 0x1c000
	s_mov_b32 s6, m0
	s_mov_b32 m0, s70
	s_nop 0
	global_load_lds_dwordx4 v1, s[0:1]
	s_mov_b32 m0, s6
	v_lshl_or_b32 v2, s8, 4, v2
	s_add_i32 s71, s29, 0x1e000
	s_mov_b32 s6, m0
	s_mov_b32 m0, s71
	s_nop 0
	global_load_lds_dwordx4 v156, s[0:1]
	s_mov_b32 m0, s6
	s_add_i32 s72, s29, 0xc000
	s_add_i32 s73, s29, 0xe000
	v_mov_b32_e32 v131, 0
	v_lshlrev_b32_e32 v130, 2, v2
	s_waitcnt vmcnt(6)
	s_cmpk_lt_u32 s4, 0x100
	v_lshl_add_u64 v[4:5], s[94:95], 0, v[130:131]
	s_mov_b64 s[0:1], 0x50800000
	v_lshlrev_b32_e32 v7, 3, v6
	s_cselect_b64 s[20:21], -1, 0
	v_lshl_add_u64 v[132:133], v[4:5], 0, s[0:1]
	s_mov_b64 s[0:1], 0x50c00000
	s_lshl_b32 s74, s8, 1
	v_add_u32_e32 v3, 0, v3
	v_lshlrev_b32_e32 v140, 1, v2
	v_mbcnt_lo_u32_b32 v2, -1, 0
	v_lshl_add_u64 v[134:135], v[4:5], 0, s[0:1]
	v_cmp_eq_u32_e64 s[6:7], 0, v6
	s_orn2_b32 s74, s74, 31
	v_lshl_or_b32 v162, s8, 5, v7
	v_mov_b32_e32 v136, s99
	v_mov_b32_e32 v137, 0
	s_add_i32 s100, s99, -1
	v_mov_b32_e32 v138, s100
	v_mov_b32_e32 v139, 0
	s_movk_i32 s75, 0x181
	v_add_u32_e32 v163, 0x10000, v3
	v_add_u32_e32 v164, 0x14000, v3
	v_add_u32_e32 v165, 0, v8
	v_add_u32_e32 v166, 0x18000, v3
	v_add_u32_e32 v167, 0x1c000, v3
	s_mov_b32 s76, 0x48600000
	s_mov_b64 s[22:23], 0x90000
	s_mov_b64 s[24:25], 0xa0000
	s_mov_b64 s[26:27], 0xb0000
	s_mov_b32 s77, 0x3c600000
	s_mov_b32 s78, 0x38600000
	s_mov_b32 s28, 0x3e6d3388
	s_mov_b32 s30, 0x3f07dc22
	s_mov_b32 s34, 0xbf3a00e3
	s_mov_b32 s36, 0x3f35f0e3
	s_mov_b32 s38, 0xbe11a98e
	s_mov_b32 s40, 0x3e027906
	s_mov_b32 s42, 0xbf38aa3b
	v_mov_b32_e32 v168, 0x3db504f3
	v_mbcnt_hi_u32_b32 v169, -1, v2
	s_mov_b32 s79, 0
	s_barrier
	s_branch .LBB0_135

; __device__ __forceinline__ unsigned xb_ld(unsigned* p)              { return __hip_atomic_load(p, __ATOMIC_RELAXED, __HIP_MEMORY_SCOPE_AGENT); }
; __device__ __forceinline__ void xcd_barrier_complete(unsigned* bar, unsigned x, unsigned& nloc, unsigned& nx) {
;     const unsigned G = gridDim.x * gridDim.y * gridDim.z;
;     unsigned sum, cnt, mine, sp = 0u;
;     for (;;) {
;         sum = 0u; cnt = 0u; mine = 0u;
; #pragma unroll
;         for (unsigned j = 0; j < 16; ++j) { const unsigned c = xb_ld(&bar[XB_XCNT(j)]); sum += c; cnt += (c > 0u) ? 1u : 0u; mine = (j == x) ? c : mine; }
; __device__ __forceinline__ void xcd_barrier(const XcdBarrier& b) {
;     asm volatile("s_waitcnt vmcnt(0)" ::: "memory");
;     __syncthreads();
;     if (threadIdx.x == 0) {
;         unsigned* bar = b.bar;
;         __builtin_amdgcn_s_waitcnt(0);
;         unsigned nloc = b.st[0], nx = b.st[1];
;         if (nloc == 0u) { xcd_barrier_complete(bar, b.x, nloc, nx); b.st[0] = nloc; b.st[1] = nx; }
.LBB0_282:
	s_mov_b32 s92, s98
	s_cmp_gt_i32 s89, 2
	s_cselect_b64 s[0:1], -1, 0
	s_and_b64 s[4:5], s[14:15], s[0:1]
	s_andn2_b64 vcc, exec, s[4:5]
	s_cbranch_vccnz .LBB0_336
	s_waitcnt vmcnt(0)
	s_waitcnt lgkmcnt(0)
	s_barrier
	s_mov_b64 s[4:5], exec
	v_readlane_b32 s6, v254, 6
	v_readlane_b32 s7, v254, 7
	s_and_b64 s[6:7], s[4:5], s[6:7]
	s_mov_b64 exec, s[6:7]
	s_cbranch_execz .LBB0_335
	s_add_i32 s3, 0, 0x23020
	v_mov_b32_e32 v1, s3
	s_waitcnt vmcnt(0) expcnt(0) lgkmcnt(0)
	ds_read_b32 v3, v1
	s_add_i32 s3, 0, 0x23024
	v_mov_b32_e32 v1, s3
	ds_read_b32 v1, v1
	s_waitcnt lgkmcnt(1)
	v_cmp_ne_u32_e32 vcc, 0, v3
	s_cbranch_vccnz .LBB0_299
	v_readlane_b32 s6, v254, 0
	v_readlane_b32 s7, v254, 1
	s_load_dwordx2 s[10:11], s[6:7], 0x4
	s_add_u32 s6, s94, 0x4200
	s_addc_u32 s7, s95, 0
	s_add_u32 s8, s94, 0x4400
	s_addc_u32 s9, s95, 0
	s_waitcnt lgkmcnt(0)
	s_mul_i32 s3, s10, s2
	s_add_u32 s10, s94, 0x4500
	s_mul_i32 s3, s3, s11
	s_addc_u32 s11, s95, 0
	s_add_u32 s12, s94, 0x4600
	s_addc_u32 s13, s95, 0
	s_add_u32 s14, s94, 0x4700
	s_addc_u32 s15, s95, 0
	s_add_u32 s16, s94, 0x4800
	s_addc_u32 s17, s95, 0
	s_add_u32 s18, s94, 0x4900
	s_addc_u32 s19, s95, 0
	s_add_u32 s20, s94, 0x4a00
	s_addc_u32 s21, s95, 0
	s_add_u32 s22, s94, 0x4b00
	s_addc_u32 s23, s95, 0
	s_add_u32 s24, s94, 0x4c00
	s_addc_u32 s25, s95, 0
	s_add_u32 s26, s94, 0x4d00
	s_addc_u32 s27, s95, 0
	s_add_u32 s28, s94, 0x4e00
	s_addc_u32 s29, s95, 0
	s_add_u32 s30, s94, 0x4f00
	s_addc_u32 s31, s95, 0
	s_add_u32 s34, s94, 0x5000
	s_addc_u32 s35, s95, 0
	s_add_u32 s36, s94, 0x5100
	s_addc_u32 s37, s95, 0
	s_add_u32 s38, s94, 0x5200
	s_addc_u32 s39, s95, 0
	s_add_u32 s40, s94, 0x5300
	s_addc_u32 s41, s95, 0
	s_mov_b32 s33, 1
	v_mov_b32_e32 v17, 0
	s_branch .LBB0_287
